# NSA tile loop: probabilities stay in the QK accumulator registers (no 16 v_mov_b64 copies), row sum as packed-add tree
# speedup vs baseline: 1.0127x; 1.0022x over previous
; __device__ __forceinline__ int crow(int r, int hi) { return (r & 3) + 8 * (r >> 2) + 4 * hi; }
; __device__ __forceinline__ void unit(LAS unsigned char* lds, const bf16* Z, const bf16* kct, const bf16* vct, bf16* OAp, int b, int g, int iq, const int tid_in) {
;     ...
;         for (int k = 0; k < ntile; ++k) {
;             const int e = TL[1 + k], n = e & 0xff, br = e >> 8, bi = k & 1;
;             if (br != curbr) {
;                 l_run += __shfl_xor(l_run, 32);
;                 const float sc = gate[1] / l_run;
; #pragma unroll
;                 for (int r = 0; r < 16; ++r) { otot[0][r] += sc * o[0][r]; otot[1][r] += sc * o[1][r]; o[0][r] = 0.f; o[1][r] = 0.f; }
;                 mref = 0.f; l_run = 0.f; curbr = br; first = true;
;             }
;             const bool sel = (br == 1) ? (((mymask >> n) & 1u) != 0u) : true;
;             const float base = sel ? (slope2 * (float)(64 * n + 4 * hi - t) - mref) : -INFINITY;
;             f32x16 p0, p1;
;             if (n == iq) {
; #pragma unroll
;                 for (int r = 0; r < 16; ++r) { const float cr = (float)((r & 3) + 8 * (r >> 2)); const int c = crow(r, hi);
;                     p0[r] = (c > tl) ? -INFINITY : fmaf(slope2, cr, base); p1[r] = (c + 32 > tl) ? -INFINITY : fmaf(slope2, cr + 32.f, base); }
;             } else if (br == 2 && n == iq - 8) {
; #pragma unroll
;                 for (int r = 0; r < 16; ++r) { const float cr = (float)((r & 3) + 8 * (r >> 2)); const int c = crow(r, hi);
;                     p0[r] = (c <= tl) ? -INFINITY : fmaf(slope2, cr, base); p1[r] = (c + 32 <= tl) ? -INFINITY : fmaf(slope2, cr + 32.f, base); }
.LBB0_484:
	v_add_f32_e32 v35, v35, v51
	v_add_f32_e32 v51, v73, v74
	v_add_f32_e32 v35, 0, v35
	v_add_f32_e32 v62, v77, v78
	v_add_f32_e32 v35, v51, v35
	v_add_f32_e32 v63, v79, v80
	v_add_f32_e32 v35, v62, v35
	v_pk_add_f32 v[36:37], v[36:37], v[38:39]
	v_add_f32_e32 v35, v63, v35
	v_add_f32_e32 v35, v37, v35
	v_pk_add_f32 v[38:39], v[40:41], v[42:43]
	v_add_f32_e32 v35, v36, v35
	v_add_f32_e32 v35, v39, v35
	v_pk_add_f32 v[40:41], v[44:45], v[46:47]
	v_add_f32_e32 v35, v38, v35
	v_add_f32_e32 v35, v41, v35
	v_pk_add_f32 v[42:43], v[48:49], v[52:53]
	v_add_f32_e32 v35, v40, v35
	v_add_f32_e32 v35, v43, v35
	v_pk_add_f32 v[44:45], v[54:55], v[56:57]
	v_add_f32_e32 v35, v42, v35
	v_add_f32_e32 v35, v45, v35
	v_pk_add_f32 v[46:47], v[58:59], v[60:61]
	v_add_f32_e32 v35, v44, v35
	v_add_f32_e32 v35, v47, v35
	s_waitcnt lgkmcnt(0)
	s_barrier
	v_add_f32_e32 v35, v46, v35
	v_pk_add_f32 v[166:167], v[34:35], 0 op_sel_hi:[1,0]
	s_cmp_eq_u32 s19, 1
	s_cbranch_scc1 .LBB0_411
	v_cmp_gt_u32_e64 s[42:43], v1, v68
	v_or_b32_e32 v1, 35, v122
	v_cmp_gt_u32_e64 s[44:45], v1, v68
	v_or_b32_e32 v1, 40, v122
	v_cmp_gt_u32_e64 s[48:49], v1, v68
	v_or_b32_e32 v1, 41, v122
	v_cmp_gt_u32_e64 s[52:53], v1, v68
	v_or_b32_e32 v1, 10, v122
	v_cmp_gt_u32_e64 s[54:55], v1, v68
	v_or_b32_e32 v1, 42, v122
	v_cmp_gt_u32_e64 s[56:57], v1, v68
	v_or_b32_e32 v1, 11, v122
	v_cmp_gt_u32_e64 s[58:59], v1, v68
	v_or_b32_e32 v1, 43, v122
	v_cmp_gt_u32_e64 s[60:61], v1, v68
	v_or_b32_e32 v1, 48, v122
	v_cmp_gt_u32_e64 s[64:65], v1, v68
	v_or_b32_e32 v1, 49, v122
	v_and_b32_e32 v34, 0xffff0000, v69
	v_cmp_gt_u32_e64 s[68:69], v1, v68
	v_or_b32_e32 v1, 18, v122
	v_mul_f32_e32 v34, 0xbfb8aa3b, v34
	v_cmp_gt_u32_e64 s[70:71], v1, v68
	v_or_b32_e32 v1, 50, v122
	v_exp_f32_e32 v34, v34
	v_cmp_gt_u32_e64 s[72:73], v1, v68
	v_or_b32_e32 v1, 19, v122
	v_cmp_gt_u32_e64 s[74:75], v1, v68
	v_or_b32_e32 v1, 51, v122
	v_cmp_gt_u32_e64 s[76:77], v1, v68
	v_or_b32_e32 v1, 56, v122
	v_cmp_gt_u32_e64 s[80:81], v1, v68
	v_or_b32_e32 v1, 57, v122
	v_add_f32_e32 v34, 1.0, v34
	v_cmp_gt_u32_e64 s[84:85], v1, v68
	v_or_b32_e32 v1, 26, v122
	v_rcp_f32_e32 v181, v34
	v_cmp_gt_u32_e64 s[86:87], v1, v68
	v_or_b32_e32 v1, 58, v122
	v_cmp_gt_u32_e64 s[88:89], v1, v68
	v_or_b32_e32 v1, 27, v122
	v_or_b32_e32 v34, 34, v122
	v_cmp_gt_u32_e64 s[90:91], v1, v68
	v_or_b32_e32 v1, 59, v122
	v_cmp_gt_u32_e64 s[0:1], v122, v68
	v_cmp_gt_u32_e64 s[4:5], v75, v68
	v_cmp_lt_u32_e64 s[6:7], v122, v68
	v_cmp_gt_u32_e64 s[8:9], v67, v68
	v_cmp_gt_u32_e64 s[38:39], v50, v68
	v_cmp_gt_u32_e64 s[40:41], v34, v68
	v_cmp_gt_u32_e64 s[46:47], v70, v68
	v_cmp_gt_u32_e64 s[50:51], v66, v68
	v_cmp_gt_u32_e64 s[62:63], v71, v68
	v_cmp_gt_u32_e64 s[66:67], v65, v68
	v_cmp_gt_u32_e64 s[78:79], v72, v68
	v_cmp_gt_u32_e64 s[82:83], v64, v68
	v_cmp_gt_u32_e64 s[92:93], v1, v68
	v_mov_b32_e32 v168, v124
	v_mov_b32_e32 v169, v124
	v_mov_b32_e32 v170, v124
	v_mov_b32_e32 v171, v124
	s_mov_b32 s28, 1
	v_readlane_b32 s94, v254, 50
	s_nop 0
	s_add_i32 s10, s94, -8
	v_mov_b32_e32 v217, s10
	ds_read_b32 v217, v217
	s_waitcnt lgkmcnt(0)
.LBB0_486:
	v_readfirstlane_b32 s12, v217
	s_ashr_i32 s95, s12, 8
	s_cmp_lg_u32 s95, s31
	s_cselect_b64 s[10:11], -1, 0
	s_cmp_eq_u32 s95, s31
	s_cbranch_scc1 .LBB0_488
	ds_bpermute_b32 v1, v172, v167
	s_mov_b32 s31, s95
	s_waitcnt lgkmcnt(0)
	v_add_f32_e32 v1, v167, v1
	v_div_scale_f32 v34, s[14:15], v1, v1, v181
	v_rcp_f32_e32 v35, v34
	v_div_scale_f32 v36, vcc, v181, v1, v181
	v_fma_f32 v37, -v34, v35, 1.0
	v_fmac_f32_e32 v35, v37, v35
	v_mul_f32_e32 v37, v36, v35
	v_fma_f32 v38, -v34, v37, v36
	v_fmac_f32_e32 v37, v38, v35
	v_fma_f32 v34, -v34, v37, v36
	v_div_fmas_f32 v34, v34, v35, v37
	v_div_fixup_f32 v34, v34, v1, v181
	v_pk_fma_f32 v[150:151], v[18:19], v[34:35], v[150:151] op_sel_hi:[1,0,1]
	v_mov_b32_e32 v18, 0
	v_pk_fma_f32 v[156:157], v[2:3], v[34:35], v[156:157] op_sel_hi:[1,0,1]
	v_pk_fma_f32 v[146:147], v[20:21], v[34:35], v[146:147] op_sel_hi:[1,0,1]
	v_pk_fma_f32 v[154:155], v[4:5], v[34:35], v[154:155] op_sel_hi:[1,0,1]
	v_pk_fma_f32 v[142:143], v[22:23], v[34:35], v[142:143] op_sel_hi:[1,0,1]
	v_pk_fma_f32 v[152:153], v[6:7], v[34:35], v[152:153] op_sel_hi:[1,0,1]
	v_pk_fma_f32 v[138:139], v[24:25], v[34:35], v[138:139] op_sel_hi:[1,0,1]
	v_pk_fma_f32 v[148:149], v[8:9], v[34:35], v[148:149] op_sel_hi:[1,0,1]
	v_pk_fma_f32 v[134:135], v[26:27], v[34:35], v[134:135] op_sel_hi:[1,0,1]
	v_pk_fma_f32 v[144:145], v[10:11], v[34:35], v[144:145] op_sel_hi:[1,0,1]
	v_pk_fma_f32 v[130:131], v[28:29], v[34:35], v[130:131] op_sel_hi:[1,0,1]
	v_pk_fma_f32 v[140:141], v[12:13], v[34:35], v[140:141] op_sel_hi:[1,0,1]
	v_pk_fma_f32 v[128:129], v[30:31], v[34:35], v[128:129] op_sel_hi:[1,0,1]
	v_pk_fma_f32 v[136:137], v[14:15], v[34:35], v[136:137] op_sel_hi:[1,0,1]
	v_pk_fma_f32 v[126:127], v[32:33], v[34:35], v[126:127] op_sel_hi:[1,0,1]
	v_pk_fma_f32 v[132:133], v[16:17], v[34:35], v[132:133] op_sel_hi:[1,0,1]
	v_mov_b32_e32 v19, v18
	v_mov_b32_e32 v20, v18
	v_mov_b32_e32 v21, v18
	v_mov_b32_e32 v22, v18
	v_mov_b32_e32 v23, v18
	v_mov_b32_e32 v24, v18
	v_mov_b32_e32 v25, v18
	v_mov_b32_e32 v26, v18
	v_mov_b32_e32 v27, v18
	v_mov_b32_e32 v28, v18
	v_mov_b32_e32 v29, v18
	v_mov_b32_e32 v30, v18
	v_mov_b32_e32 v31, v18
	v_mov_b32_e32 v32, v18
	v_mov_b32_e32 v33, v18
	v_mov_b32_e32 v2, v18
	v_mov_b32_e32 v3, v18
	v_mov_b32_e32 v4, v18
	v_mov_b32_e32 v5, v18
	v_mov_b32_e32 v6, v18
	v_mov_b32_e32 v7, v18
	v_mov_b32_e32 v8, v18
	v_mov_b32_e32 v9, v18
	v_mov_b32_e32 v10, v18
	v_mov_b32_e32 v11, v18
	v_mov_b32_e32 v12, v18
	v_mov_b32_e32 v13, v18
	v_mov_b32_e32 v14, v18
	v_mov_b32_e32 v15, v18
	v_mov_b32_e32 v16, v18
	v_mov_b32_e32 v17, v18
	v_mov_b32_e32 v166, v18
	v_mov_b32_e32 v167, v18

; #define LAS __attribute__((address_space(3)))
; #define MFMA32(a, b, c) __builtin_amdgcn_mfma_f32_32x32x16_bf16((a), (b), (c), 0, 0, 0)
; __device__ __forceinline__ void unit(LAS unsigned char* lds, const bf16* Z, const bf16* kct, const bf16* vct, bf16* OAp, int b, int g, int iq, const int tid_in) {
;     ...
;             for (int d0 = 0; d0 < 4; ++d0) {
;                 const bf16x8 k0 = *(const LAS bf16x8*)(KSb[bi] + r32 * KST + 16 * d0 + 8 * hi);
;                 const bf16x8 k1 = *(const LAS bf16x8*)(KSb[bi] + (r32 + 32) * KST + 16 * d0 + 8 * hi);
;                 p0 = MFMA32(k0, qr[d0], p0); p1 = MFMA32(k1, qr[d0], p1); }
;             float mx = fmaxf(p0[0], p1[0]);
; #pragma unroll
;             for (int r = 1; r < 16; ++r) mx = fmaxf(mx, fmaxf(p0[r], p1[r]));
;             mx = fmaxf(mx, __shfl_xor(mx, 32));
;             if (first) {
;                 const float dl = (mx == -INFINITY) ? 0.f : mx; mref += dl;
; #pragma unroll
;                 for (int r = 0; r < 16; ++r) { p0[r] -= dl; p1[r] -= dl; }
;                 first = false;
.LBB0_496:
	s_bitcmp1_b32 s28, 0
	s_cselect_b32 s12, s37, 0
	v_add3_u32 v1, s12, v179, v180
	ds_read_b128 v[66:69], v1
	ds_read_b128 v[70:73], v1 offset:32
	s_andn2_b64 vcc, exec, s[10:11]
	s_mov_b64 s[10:11], -1
	s_waitcnt lgkmcnt(1)
	v_mfma_f32_32x32x16_bf16 v[34:49], v[66:69], v[98:101], v[34:49]
	ds_read_b128 v[66:69], v1 offset:4608
	ds_read_b128 v[74:77], v1 offset:4640
	s_waitcnt lgkmcnt(1)
	v_mfma_f32_32x32x16_bf16 v[50:65], v[66:69], v[98:101], v[50:65]
	v_mfma_f32_32x32x16_bf16 v[34:49], v[70:73], v[102:105], v[34:49]
	ds_read_b128 v[66:69], v1 offset:64
	ds_read_b128 v[70:73], v1 offset:96
	s_waitcnt lgkmcnt(2)
	v_mfma_f32_32x32x16_bf16 v[50:65], v[74:77], v[102:105], v[50:65]
	s_waitcnt lgkmcnt(1)
	v_mfma_f32_32x32x16_bf16 v[34:49], v[66:69], v[106:109], v[34:49]
	ds_read_b128 v[66:69], v1 offset:4672
	ds_read_b128 v[74:77], v1 offset:4704
	s_waitcnt lgkmcnt(1)
	v_mfma_f32_32x32x16_bf16 v[50:65], v[66:69], v[106:109], v[50:65]
	v_mfma_f32_32x32x16_bf16 v[34:49], v[70:73], v[110:113], v[34:49]
	s_waitcnt lgkmcnt(0)
	v_mfma_f32_32x32x16_bf16 v[50:65], v[74:77], v[110:113], v[50:65]
	s_nop 9
	v_max3_f32 v1, v34, v35, v36
	v_max3_f32 v66, v37, v38, v39
	v_max3_f32 v67, v50, v51, v52
	v_max3_f32 v68, v53, v54, v55
	v_max3_f32 v1, v1, v40, v41
	v_max3_f32 v66, v66, v42, v43
	v_max3_f32 v67, v67, v56, v57
	v_max3_f32 v68, v68, v58, v59
	v_max3_f32 v1, v1, v44, v45
	v_max3_f32 v66, v66, v46, v47
	v_max3_f32 v67, v67, v60, v61
	v_max3_f32 v68, v68, v62, v63
	v_max3_f32 v1, v1, v48, v49
	v_max3_f32 v67, v67, v64, v65
	v_max3_f32 v1, v1, v66, v67
	v_max_f32_e32 v1, v1, v68
	v_mov_b32_e32 v66, v1
	s_nop 1
	v_permlane32_swap_b32_e32 v66, v1
	v_max_f32_e32 v1, v66, v1
	s_cbranch_vccnz .LBB0_498
	s_mov_b32 s10, 0xff800000
	v_cmp_neq_f32_e32 vcc, s10, v1
	s_mov_b64 s[10:11], 0
	s_nop 0
	v_cndmask_b32_e32 v125, 0, v1, vcc
	v_sub_f32_e32 v49, v49, v125
	v_sub_f32_e32 v48, v48, v125
	v_sub_f32_e32 v47, v47, v125
	v_sub_f32_e32 v46, v46, v125
	v_sub_f32_e32 v45, v45, v125
	v_sub_f32_e32 v44, v44, v125
	v_sub_f32_e32 v43, v43, v125
	v_sub_f32_e32 v42, v42, v125
	v_sub_f32_e32 v41, v41, v125
	v_sub_f32_e32 v40, v40, v125
	v_sub_f32_e32 v39, v39, v125
	v_sub_f32_e32 v38, v38, v125
	v_sub_f32_e32 v37, v37, v125
	v_sub_f32_e32 v36, v36, v125
	v_sub_f32_e32 v35, v35, v125
	v_sub_f32_e32 v34, v34, v125
	v_sub_f32_e32 v65, v65, v125
	v_sub_f32_e32 v64, v64, v125
	v_sub_f32_e32 v63, v63, v125
	v_sub_f32_e32 v62, v62, v125
	v_sub_f32_e32 v61, v61, v125
	v_sub_f32_e32 v60, v60, v125
	v_sub_f32_e32 v59, v59, v125
	v_sub_f32_e32 v58, v58, v125
	v_sub_f32_e32 v57, v57, v125
	v_sub_f32_e32 v56, v56, v125
	v_sub_f32_e32 v55, v55, v125
	v_sub_f32_e32 v54, v54, v125
	v_sub_f32_e32 v53, v53, v125
	v_sub_f32_e32 v52, v52, v125
	v_sub_f32_e32 v51, v51, v125
	v_sub_f32_e32 v50, v50, v125
	v_add_f32_e32 v125, v166, v125

; __device__ __forceinline__ void unit(LAS unsigned char* lds, const bf16* Z, const bf16* kct, const bf16* vct, bf16* OAp, int b, int g, int iq, const int tid_in) {
;     ...
;             } else if (__any(mx > 8.0f)) {
;                 const float dl = fmaxf(mx, 0.f); mref += dl;
;                 const float f = __builtin_amdgcn_exp2f(-dl); l_run *= f;
; #pragma unroll
;                 for (int r = 0; r < 16; ++r) { p0[r] -= dl; p1[r] -= dl; o[0][r] *= f; o[1][r] *= f; }
;             }
.LBB0_501:
	s_branch .LBB0_503

; #define LAS __attribute__((address_space(3)))
; __device__ __forceinline__ unsigned cvt_pk_bf16(float lo, float hi) { f32x2_t v = {lo, hi}; bf16x2_t b = __builtin_convertvector(v, bf16x2_t); return __builtin_bit_cast(unsigned, b); }
; #define MFMA32(a, b, c) __builtin_amdgcn_mfma_f32_32x32x16_bf16((a), (b), (c), 0, 0, 0)
; __device__ __forceinline__ void unit(LAS unsigned char* lds, const bf16* Z, const bf16* kct, const bf16* vct, bf16* OAp, int b, int g, int iq, const int tid_in) {
;     ...
;             float rs = 0.f;
; #pragma unroll
;             for (int r = 0; r < 16; ++r) { p0[r] = __builtin_amdgcn_exp2f(p0[r]); p1[r] = __builtin_amdgcn_exp2f(p1[r]); rs += p0[r] + p1[r]; }
;             l_run += rs;
; #pragma unroll
;             for (int s = 0; s < 4; ++s) {
;                 u32x4 pw;
;                 if (s < 2) { const int rb = 8 * s; pw.x = cvt_pk_bf16(p0[rb + 0], p0[rb + 1]); pw.y = cvt_pk_bf16(p0[rb + 2], p0[rb + 3]); pw.z = cvt_pk_bf16(p0[rb + 4], p0[rb + 5]); pw.w = cvt_pk_bf16(p0[rb + 6], p0[rb + 7]); }
;                 else { const int rb = 8 * (s - 2); pw.x = cvt_pk_bf16(p1[rb + 0], p1[rb + 1]); pw.y = cvt_pk_bf16(p1[rb + 2], p1[rb + 3]); pw.z = cvt_pk_bf16(p1[rb + 4], p1[rb + 5]); pw.w = cvt_pk_bf16(p1[rb + 6], p1[rb + 7]); }
;                 const bf16x8 pa = __builtin_bit_cast(bf16x8, pw);
; #pragma unroll
;                 for (int db = 0; db < 2; ++db) { const bf16x8 vf = *(const LAS bf16x8*)(VTb[bi] + (32 * db + r32) * KST + 16 * s + 8 * hi); o[db] = MFMA32(vf, pa, o[db]); } }
;             if (k + 1 < ntile) { NSA_STORE(bi ^ 1); if (k + 2 < ntile) NSA_LOAD(TL[3 + k]); }
;             asm volatile("s_waitcnt lgkmcnt(0)\n\ts_barrier" ::: "memory");
.LBB0_503:
	s_and_b32 s11, s28, 1
	s_add_i32 s10, s28, 1
	s_cmp_lg_u32 s11, 0
	s_mov_b32 s12, 0x9000
	s_cselect_b32 s12, s12, 0x2400
	s_add_i32 s12, s12, 0
	v_exp_f32_e32 v34, v34
	v_exp_f32_e32 v35, v35
	v_exp_f32_e32 v36, v36
	v_exp_f32_e32 v37, v37
	v_exp_f32_e32 v38, v38
	v_exp_f32_e32 v39, v39
	v_exp_f32_e32 v40, v40
	v_exp_f32_e32 v41, v41
	v_add3_u32 v216, s12, v120, v179
	v_exp_f32_e32 v42, v42
	v_exp_f32_e32 v43, v43
	v_exp_f32_e32 v44, v44
	v_exp_f32_e32 v45, v45
	ds_read_b128 v[70:73], v216
	ds_read_b128 v[74:77], v216 offset:32
	v_cvt_pk_bf16_f32 v66, v34, v35
	v_cvt_pk_bf16_f32 v67, v36, v37
	v_cvt_pk_bf16_f32 v68, v38, v39
	v_cvt_pk_bf16_f32 v69, v40, v41
	v_exp_f32_e32 v46, v46
	v_exp_f32_e32 v47, v47
	s_waitcnt lgkmcnt(1)
	v_mfma_f32_32x32x16_bf16 v[18:33], v[70:73], v[66:69], v[18:33]
	ds_read_b128 v[70:73], v216 offset:4608
	v_exp_f32_e32 v48, v48
	v_exp_f32_e32 v49, v49
	v_exp_f32_e32 v50, v50
	v_exp_f32_e32 v51, v51
	v_exp_f32_e32 v52, v52
	v_exp_f32_e32 v53, v53
	s_waitcnt lgkmcnt(0)
	v_mfma_f32_32x32x16_bf16 v[2:17], v[70:73], v[66:69], v[2:17]
	ds_read_b128 v[70:73], v216 offset:4640
	v_cvt_pk_bf16_f32 v66, v42, v43
	v_cvt_pk_bf16_f32 v67, v44, v45
	v_cvt_pk_bf16_f32 v68, v46, v47
	v_cvt_pk_bf16_f32 v69, v48, v49
	v_exp_f32_e32 v54, v54
	v_exp_f32_e32 v55, v55
	s_waitcnt lgkmcnt(0)
	v_mfma_f32_32x32x16_bf16 v[2:17], v[70:73], v[66:69], v[2:17]
	ds_read_b128 v[70:73], v216 offset:64
	v_exp_f32_e32 v56, v56
	v_exp_f32_e32 v57, v57
	v_exp_f32_e32 v58, v58
	v_exp_f32_e32 v59, v59
	v_exp_f32_e32 v60, v60
	v_exp_f32_e32 v61, v61
	v_mfma_f32_32x32x16_bf16 v[18:33], v[74:77], v[66:69], v[18:33]
	v_cvt_pk_bf16_f32 v66, v50, v51
	v_cvt_pk_bf16_f32 v67, v52, v53
	v_cvt_pk_bf16_f32 v68, v54, v55
	v_cvt_pk_bf16_f32 v69, v56, v57
	v_exp_f32_e32 v62, v62
	v_exp_f32_e32 v63, v63
	v_exp_f32_e32 v64, v64
	s_waitcnt lgkmcnt(0)
	v_mfma_f32_32x32x16_bf16 v[18:33], v[70:73], v[66:69], v[18:33]
	ds_read_b128 v[70:73], v216 offset:4672
	v_exp_f32_e32 v65, v65
	s_cmp_ge_i32 s10, s19
	s_waitcnt lgkmcnt(0)
	v_mfma_f32_32x32x16_bf16 v[2:17], v[70:73], v[66:69], v[2:17]
	ds_read_b128 v[70:73], v216 offset:96
	v_cvt_pk_bf16_f32 v66, v58, v59
	v_cvt_pk_bf16_f32 v67, v60, v61
	v_cvt_pk_bf16_f32 v68, v62, v63
	v_cvt_pk_bf16_f32 v69, v64, v65
	s_waitcnt lgkmcnt(0)
	s_nop 0
	v_mfma_f32_32x32x16_bf16 v[18:33], v[70:73], v[66:69], v[18:33]
	ds_read_b128 v[70:73], v216 offset:4704
	s_waitcnt lgkmcnt(0)
	v_mfma_f32_32x32x16_bf16 v[2:17], v[70:73], v[66:69], v[2:17]
	s_cbranch_scc1 .LBB0_506
	s_add_i32 s12, 0, 0x9000
	s_add_i32 s13, 0, 0x2400
	s_cmp_eq_u32 s11, 0
	s_cselect_b32 s11, s37, 0
	v_add3_u32 v216, s11, v175, v186
	s_cselect_b32 s11, s12, s13
	s_waitcnt vmcnt(2)
	ds_write_b128 v216, v[114:117]
	v_add3_u32 v216, s11, v176, v177
	s_waitcnt vmcnt(0)
	v_lshlrev_b32_e32 v66, 16, v160
	s_mov_b32 s11, 0xffff
	v_lshrrev_b32_e32 v67, 16, v158
	v_and_or_b32 v66, v158, s11, v66
	v_and_or_b32 v67, v160, s27, v67
	ds_write2_b32 v216, v66, v67 offset1:36
	v_lshlrev_b32_e32 v66, 16, v161
	v_and_or_b32 v66, v159, s11, v66
	v_lshrrev_b32_e32 v67, 16, v159
	s_add_i32 s11, s28, 2
	v_and_or_b32 v67, v161, s27, v67
	s_cmp_ge_i32 s11, s19
	ds_write2_b32 v216, v66, v67 offset0:72 offset1:108
	s_cbranch_scc1 .LBB0_506
	v_mov_b32_e32 v216, s94
	ds_read_b32 v216, v216
	s_waitcnt lgkmcnt(0)
	v_readfirstlane_b32 s11, v216
	s_lshl_b32 s12, s11, 6
	s_and_b32 s12, s12, 0x3fc0
	s_and_b32 s11, s11, 0xffffff00
	s_add_i32 s14, s12, s22
	v_add_u32_e32 v216, s14, v119
	s_cmpk_eq_i32 s11, 0x100
	v_mad_i64_i32 v[66:67], s[12:13], v216, s26, v[162:163]
	s_cselect_b32 s28, 0xc00, s97
	v_or_b32_e32 v216, s14, v174
	s_movk_i32 s11, 0xe00
	v_lshl_add_u64 v[66:67], v[66:67], 0, s[28:29]
	s_cselect_b32 s28, s11, 0x1200
	v_mad_i64_i32 v[68:69], s[12:13], v216, s26, v[164:165]
	v_lshl_add_u64 v[68:69], v[68:69], 0, s[28:29]
	global_load_dwordx4 v[114:117], v[66:67], off
	global_load_dwordx2 v[158:159], v[68:69], off
	v_add_co_u32_e32 v66, vcc, 0x4000, v68
	s_nop 1
	v_addc_co_u32_e32 v67, vcc, 0, v69, vcc
	global_load_dwordx2 v[160:161], v[66:67], off offset:1536
.LBB0_506:
	v_pk_add_f32 v[34:35], v[34:35], v[36:37]
	v_pk_add_f32 v[38:39], v[38:39], v[40:41]
	v_pk_add_f32 v[42:43], v[42:43], v[44:45]
	v_pk_add_f32 v[46:47], v[46:47], v[48:49]
	v_pk_add_f32 v[50:51], v[50:51], v[52:53]
	v_pk_add_f32 v[54:55], v[54:55], v[56:57]
	v_pk_add_f32 v[58:59], v[58:59], v[60:61]
	v_pk_add_f32 v[62:63], v[62:63], v[64:65]
	v_pk_add_f32 v[34:35], v[34:35], v[38:39]
	v_pk_add_f32 v[42:43], v[42:43], v[46:47]
	v_pk_add_f32 v[50:51], v[50:51], v[54:55]
	v_pk_add_f32 v[58:59], v[58:59], v[62:63]
	v_pk_add_f32 v[34:35], v[34:35], v[42:43]
	v_pk_add_f32 v[50:51], v[50:51], v[58:59]
	v_pk_add_f32 v[34:35], v[34:35], v[50:51]
	s_add_i32 s11, s94, -4
	v_mov_b32_e32 v217, s11
	ds_read_b32 v217, v217
	s_waitcnt lgkmcnt(0)
	s_barrier
	v_add_f32_e32 v1, v34, v35
	s_add_i32 s94, s94, 4
	v_add_f32_e32 v167, v167, v1
	s_cmp_lg_u32 s19, s10
	s_cbranch_scc0 .LBB0_411
	s_mov_b32 s28, s10
	s_branch .LBB0_486
